# QKV K-loop: one static s_setprio 1 for waves 4-7 instead of per-half priority toggles on all waves
# speedup vs baseline: 1.0006x; 1.0006x over previous
.Lqk_bias_done:
	v_lshlrev_b32_e32 v5, 7, v0
	v_lshlrev_b32_e32 v2, 3, v2
	s_mov_b32 s7, 0x1fc00
	v_mov_b32_e32 v6, 0x10000
	s_add_u32 s16, s24, s18
	v_and_b32_e32 v3, 56, v2
	v_and_b32_e32 v4, 0xfc00, v5
	v_bitop3_b32 v5, v5, s7, v6 bitop3:0xc8
	v_lshlrev_b32_e32 v8, 8, v0
	s_mov_b32 s7, 0x3f800
	v_mov_b32_e32 v7, 0x20000
	s_addc_u32 s17, s25, s19
	v_or_b32_e32 v2, v4, v3
	v_bitop3_b32 v7, v8, s7, v7 bitop3:0xc8
	s_mov_b32 s7, 0x7f800
	v_mov_b32_e32 v11, 0x60000
	s_waitcnt lgkmcnt(0)
	s_add_u32 s22, s0, s2
	v_and_b32_e32 v6, 0x1f800, v8
	v_bitop3_b32 v8, v8, s7, v11 bitop3:0xc8
	v_lshlrev_b32_e32 v12, 1, v2
	v_mov_b32_e32 v2, 0
	v_readfirstlane_b32 s7, v79
	v_or_b32_e32 v9, v5, v3
	s_addc_u32 s23, s1, s3
	v_mov_b32_e32 v13, v2
	s_mov_b32 m0, s7
	v_lshl_add_u64 v[14:15], s[22:23], 0, v[12:13]
	global_load_lds_dwordx4 v12, s[22:23]
	v_lshlrev_b32_e32 v12, 1, v9
	v_or_b32_e32 v9, 0x2000, v79
	v_or_b32_e32 v10, v6, v3
	v_readfirstlane_b32 s7, v9
	v_or_b32_e32 v9, 0x4000, v79
	s_mov_b32 m0, s7
	v_readfirstlane_b32 s7, v9
	v_or_b32_e32 v9, 0x6000, v79
	v_or_b32_e32 v18, v7, v3
	v_lshlrev_b32_e32 v10, 1, v10
	global_load_lds_dwordx4 v12, s[22:23]
	s_mov_b32 m0, s7
	v_readfirstlane_b32 s7, v9
	v_or_b32_e32 v9, 0x8000, v79
	v_mov_b32_e32 v11, v2
	global_load_lds_dwordx4 v10, s[16:17]
	v_lshlrev_b32_e32 v18, 1, v18
	s_mov_b32 m0, s7
	v_readfirstlane_b32 s7, v9
	v_or_b32_e32 v9, 0xa000, v79
	v_or_b32_e32 v22, v8, v3
	v_lshl_add_u64 v[16:17], s[22:23], 0, v[12:13]
	v_lshl_add_u64 v[12:13], s[16:17], 0, v[10:11]
	v_mov_b32_e32 v19, v2
	global_load_lds_dwordx4 v18, s[16:17]
	v_or_b32_e32 v10, 0x80000, v10
	s_mov_b32 m0, s7
	v_readfirstlane_b32 s7, v9
	v_lshl_add_u64 v[20:21], s[16:17], 0, v[18:19]
	v_lshl_add_u64 v[18:19], s[16:17], 0, v[10:11]
	global_load_lds_dwordx4 v10, s[16:17]
	v_lshlrev_b32_e32 v10, 1, v22
	s_mov_b32 m0, s7
	v_or_b32_e32 v9, 0xc000, v79
	v_lshl_add_u64 v[22:23], s[16:17], 0, v[10:11]
	global_load_lds_dwordx4 v10, s[16:17]
	s_mov_b64 s[16:17], 0x80
	v_readfirstlane_b32 s7, v9
	v_or_b32_e32 v9, 0xe000, v79
	v_lshl_add_u64 v[10:11], v[14:15], 0, s[16:17]
	s_mov_b32 m0, s7
	v_readfirstlane_b32 s7, v9
	v_or_b32_e32 v9, 0x10000, v79
	global_load_lds_dwordx4 v[10:11], off
	v_lshl_add_u64 v[10:11], v[16:17], 0, s[16:17]
	s_mov_b32 m0, s7
	v_readfirstlane_b32 s7, v9
	v_or_b32_e32 v9, 0x12000, v79
	global_load_lds_dwordx4 v[10:11], off
	v_lshl_add_u64 v[10:11], v[12:13], 0, s[16:17]
	s_mov_b32 m0, s7
	v_readfirstlane_b32 s7, v9
	v_or_b32_e32 v9, 0x14000, v79
	global_load_lds_dwordx4 v[10:11], off
	v_lshl_add_u64 v[10:11], v[20:21], 0, s[16:17]
	s_mov_b32 m0, s7
	v_readfirstlane_b32 s7, v9
	v_or_b32_e32 v9, 0x16000, v79
	global_load_lds_dwordx4 v[10:11], off
	v_lshl_add_u64 v[10:11], v[18:19], 0, s[16:17]
	s_mov_b32 m0, s7
	v_readfirstlane_b32 s7, v9
	global_load_lds_dwordx4 v[10:11], off
	v_lshl_add_u64 v[10:11], v[22:23], 0, s[16:17]
	s_mov_b32 m0, s7
	s_nop 0
	global_load_lds_dwordx4 v[10:11], off
	s_cmp_lt_i32 s20, 16
	s_cselect_b64 s[16:17], -1, 0
	s_cmp_gt_i32 s20, 15
	v_bfe_u32 v9, v0, 6, 2
	s_cselect_b64 vcc, -1, 0
	v_cndmask_b32_e32 v83, v78, v9, vcc
	v_cndmask_b32_e32 v9, v9, v78, vcc
	s_and_b64 s[22:23], vcc, exec
	v_lshl_or_b32 v80, v9, 6, v42
	v_bfe_u32 v9, v0, 1, 3
	s_cselect_b32 s26, 0x2000, 0
	s_cselect_b32 s27, 0, 0x2000
	v_bitop3_b32 v9, v1, v9, 4 bitop3:0x36
	s_add_u32 s18, s24, s18
	v_lshlrev_b32_e32 v84, 4, v9
	v_add_lshl_u32 v8, v8, v3, 1
	v_mov_b32_e32 v9, v2
	s_addc_u32 s19, s25, s19
	v_lshl_add_u64 v[8:9], s[18:19], 0, v[8:9]
	s_mov_b64 s[22:23], 0x100
	v_lshl_add_u64 v[66:67], v[8:9], 0, s[22:23]
	v_add_lshl_u32 v8, v7, v3, 1
	v_mov_b32_e32 v9, v2
	v_lshl_add_u64 v[8:9], s[18:19], 0, v[8:9]
	v_add_lshl_u32 v6, v6, v3, 1
	v_mov_b32_e32 v7, v2
	v_lshl_add_u64 v[68:69], v[8:9], 0, s[22:23]
	v_lshl_add_u64 v[8:9], s[18:19], 0, v[6:7]
	v_or_b32_e32 v6, 0x80000, v6
	v_lshlrev_b32_e32 v82, 6, v83
	v_lshl_add_u64 v[6:7], s[18:19], 0, v[6:7]
	s_add_u32 s0, s0, s2
	v_or_b32_e32 v10, v82, v42
	v_lshl_add_u64 v[72:73], v[6:7], 0, s[22:23]
	v_add_lshl_u32 v6, v5, v3, 1
	v_mov_b32_e32 v7, v2
	s_addc_u32 s1, s1, s3
	v_add_lshl_u32 v4, v4, v3, 1
	v_mov_b32_e32 v5, v2
	v_lshlrev_b32_e32 v86, 7, v10
	v_bitop3_b32 v10, v43, v1, 7 bitop3:0x6c
	v_lshl_add_u64 v[6:7], s[0:1], 0, v[6:7]
	v_lshl_add_u64 v[4:5], s[0:1], 0, v[4:5]
	v_lshlrev_b32_e32 v85, 4, v10
	v_lshlrev_b32_e32 v81, 7, v80
	v_lshl_add_u64 v[70:71], v[8:9], 0, s[22:23]
	v_lshl_add_u64 v[74:75], v[6:7], 0, s[22:23]
	v_lshl_add_u64 v[76:77], v[4:5], 0, s[22:23]
	s_mov_b32 s18, 2
	s_mov_b64 s[0:1], 0
	s_lshl_b32 s3, s26, 1
	s_lshl_b32 s2, s27, 1
	v_mov_b32_e32 v3, v2
	v_mov_b32_e32 v4, v2
	v_mov_b32_e32 v5, v2
	v_mov_b32_e32 v6, v2
	v_mov_b32_e32 v7, v2
	v_mov_b32_e32 v8, v2
	v_mov_b32_e32 v9, v2
	v_mov_b32_e32 v10, v2
	v_mov_b32_e32 v11, v2
	v_mov_b32_e32 v12, v2
	v_mov_b32_e32 v13, v2
	v_mov_b32_e32 v14, v2
	v_mov_b32_e32 v15, v2
	v_mov_b32_e32 v16, v2
	v_mov_b32_e32 v17, v2
	v_mov_b32_e32 v18, v2
	v_mov_b32_e32 v19, v2
	v_mov_b32_e32 v20, v2
	v_mov_b32_e32 v21, v2
	v_mov_b32_e32 v22, v2
	v_mov_b32_e32 v23, v2
	v_mov_b32_e32 v24, v2
	v_mov_b32_e32 v25, v2
	v_mov_b32_e32 v26, v2
	v_mov_b32_e32 v27, v2
	v_mov_b32_e32 v28, v2
	v_mov_b32_e32 v29, v2
	v_mov_b32_e32 v30, v2
	v_mov_b32_e32 v31, v2
	v_mov_b32_e32 v32, v2
	v_mov_b32_e32 v33, v2
	v_mov_b32_e32 v34, v2
	v_mov_b32_e32 v35, v2
	v_mov_b32_e32 v36, v2
	v_mov_b32_e32 v37, v2
	v_mov_b32_e32 v38, v2
	v_mov_b32_e32 v39, v2
	v_mov_b32_e32 v40, v2
	v_mov_b32_e32 v41, v2
	v_mov_b32_e32 v42, v2
	v_mov_b32_e32 v43, v2
	v_mov_b32_e32 v44, v2
	v_mov_b32_e32 v45, v2
	v_mov_b32_e32 v46, v2
	v_mov_b32_e32 v47, v2
	v_mov_b32_e32 v48, v2
	v_mov_b32_e32 v49, v2
	v_mov_b32_e32 v50, v2
	v_mov_b32_e32 v51, v2
	v_mov_b32_e32 v52, v2
	v_mov_b32_e32 v53, v2
	v_mov_b32_e32 v54, v2
	v_mov_b32_e32 v55, v2
	v_mov_b32_e32 v56, v2
	v_mov_b32_e32 v57, v2
	v_mov_b32_e32 v58, v2
	v_mov_b32_e32 v59, v2
	v_mov_b32_e32 v60, v2
	v_mov_b32_e32 v61, v2
	v_mov_b32_e32 v62, v2
	v_mov_b32_e32 v63, v2
	v_mov_b32_e32 v64, v2
	v_mov_b32_e32 v65, v2
	v_readfirstlane_b32 s44, v79
	s_mov_b32 s45, 0
	s_mov_b32 s46, 1
	s_mov_b32 s48, 0
	s_mov_b64 s[0:1], 0
	s_add_u32 s49, s44, 0x18000
	s_mov_b32 m0, s49
	v_lshl_add_u64 v[124:125], v[76:77], 0, s[0:1]
	global_load_lds_dwordx4 v[124:125], off
	s_add_u32 m0, s49, 0x2000
	v_lshl_add_u64 v[124:125], v[74:75], 0, s[0:1]
	global_load_lds_dwordx4 v[124:125], off
	s_add_u32 m0, s49, 0x4000
	v_lshl_add_u64 v[124:125], v[70:71], 0, s[0:1]
	global_load_lds_dwordx4 v[124:125], off
	s_add_u32 m0, s49, 0x6000
	v_lshl_add_u64 v[124:125], v[68:69], 0, s[0:1]
	global_load_lds_dwordx4 v[124:125], off
	s_add_u32 m0, s49, 0x8000
	v_lshl_add_u64 v[124:125], v[72:73], 0, s[0:1]
	global_load_lds_dwordx4 v[124:125], off
	s_add_u32 m0, s49, 0xa000
	v_lshl_add_u64 v[124:125], v[66:67], 0, s[0:1]
	global_load_lds_dwordx4 v[124:125], off
	s_mov_b64 s[0:1], 0x80
	s_waitcnt vmcnt(12)
	s_barrier
	s_mov_b32 s46, 0
	s_mul_i32 s49, s46, 0xc000
	s_add_u32 s50, s49, s3
	s_add_u32 s51, s49, s2
	v_add3_u32 v120, s50, v86, v85
	v_add3_u32 v121, s50, v86, v84
	v_add3_u32 v122, s51, v81, v85
	v_add3_u32 v123, s51, v81, v84
	ds_read_b128 v[88:91], v120
	ds_read_b128 v[92:95], v120 offset:2048
	ds_read_b128 v[96:99], v120 offset:4096
	ds_read_b128 v[100:103], v120 offset:6144
	ds_read_b128 v[104:107], v122
	ds_read_b128 v[108:111], v122 offset:2048
	ds_read_b128 v[112:115], v122 offset:4096
	ds_read_b128 v[116:119], v122 offset:6144
	ds_read_b128 v[144:147], v121
	ds_read_b128 v[148:151], v121 offset:2048
	ds_read_b128 v[152:155], v121 offset:4096
	ds_read_b128 v[156:159], v121 offset:6144
	ds_read_b128 v[160:163], v123
	ds_read_b128 v[164:167], v123 offset:2048
	ds_read_b128 v[168:171], v123 offset:4096
	ds_read_b128 v[172:175], v123 offset:6144
	s_mov_b32 s46, 1
	s_cmp_lt_u32 s44, 0x1000
	s_cbranch_scc1 .Lqk_prio_skip
	s_setprio 1
.Lqk_prio_skip:
.LBB1_36:
	s_waitcnt vmcnt(6)
	s_waitcnt lgkmcnt(0)
	s_barrier
	s_mul_i32 s49, s46, 0xc000
	s_add_u32 s50, s49, s3
	s_add_u32 s51, s49, s2
	v_add3_u32 v120, s50, v86, v85
	v_add3_u32 v121, s50, v86, v84
	v_add3_u32 v122, s51, v81, v85
	v_add3_u32 v123, s51, v81, v84
	s_mul_i32 s49, s45, 0xc000
	s_add_u32 s49, s49, s44
	ds_read_b128 v[176:179], v120
	ds_read_b128 v[180:183], v120 offset:2048
	ds_read_b128 v[184:187], v120 offset:4096
	ds_read_b128 v[188:191], v120 offset:6144
	v_mfma_f32_16x16x32_f16 v[62:65], v[88:91], v[104:107], v[62:65]
	ds_read_b128 v[192:195], v122
	v_mfma_f32_16x16x32_f16 v[58:61], v[88:91], v[108:111], v[58:61]
	ds_read_b128 v[196:199], v122 offset:2048
	v_mfma_f32_16x16x32_f16 v[54:57], v[88:91], v[112:115], v[54:57]
	ds_read_b128 v[200:203], v122 offset:4096
	v_mfma_f32_16x16x32_f16 v[50:53], v[88:91], v[116:119], v[50:53]
	ds_read_b128 v[204:207], v122 offset:6144
	v_mfma_f32_16x16x32_f16 v[46:49], v[92:95], v[104:107], v[46:49]
	ds_read_b128 v[208:211], v121
	v_mfma_f32_16x16x32_f16 v[42:45], v[92:95], v[108:111], v[42:45]
	ds_read_b128 v[212:215], v121 offset:2048
	v_mfma_f32_16x16x32_f16 v[38:41], v[92:95], v[112:115], v[38:41]
	ds_read_b128 v[216:219], v121 offset:4096
	v_mfma_f32_16x16x32_f16 v[34:37], v[92:95], v[116:119], v[34:37]
	ds_read_b128 v[220:223], v121 offset:6144
	v_mfma_f32_16x16x32_f16 v[30:33], v[96:99], v[104:107], v[30:33]
	ds_read_b128 v[224:227], v123
	v_mfma_f32_16x16x32_f16 v[26:29], v[96:99], v[108:111], v[26:29]
	ds_read_b128 v[228:231], v123 offset:2048
	v_mfma_f32_16x16x32_f16 v[22:25], v[96:99], v[112:115], v[22:25]
	ds_read_b128 v[232:235], v123 offset:4096
	v_mfma_f32_16x16x32_f16 v[18:21], v[96:99], v[116:119], v[18:21]
	ds_read_b128 v[236:239], v123 offset:6144
	v_mfma_f32_16x16x32_f16 v[14:17], v[100:103], v[104:107], v[14:17]
	v_mfma_f32_16x16x32_f16 v[10:13], v[100:103], v[108:111], v[10:13]
	v_mfma_f32_16x16x32_f16 v[6:9], v[100:103], v[112:115], v[6:9]
	s_mov_b32 m0, s49
	v_lshl_add_u64 v[124:125], v[76:77], 0, s[0:1]
	global_load_lds_dwordx4 v[124:125], off
	v_mfma_f32_16x16x32_f16 v[2:5], v[100:103], v[116:119], v[2:5]
	v_mfma_f32_16x16x32_f16 v[62:65], v[144:147], v[160:163], v[62:65]
	v_mfma_f32_16x16x32_f16 v[58:61], v[144:147], v[164:167], v[58:61]
	s_add_u32 m0, s49, 0x2000
	v_lshl_add_u64 v[124:125], v[74:75], 0, s[0:1]
	global_load_lds_dwordx4 v[124:125], off
	v_mfma_f32_16x16x32_f16 v[54:57], v[144:147], v[168:171], v[54:57]
	v_mfma_f32_16x16x32_f16 v[50:53], v[144:147], v[172:175], v[50:53]
	v_mfma_f32_16x16x32_f16 v[46:49], v[148:151], v[160:163], v[46:49]
	s_add_u32 m0, s49, 0x4000
	v_lshl_add_u64 v[124:125], v[70:71], 0, s[0:1]
	global_load_lds_dwordx4 v[124:125], off
	v_mfma_f32_16x16x32_f16 v[42:45], v[148:151], v[164:167], v[42:45]
	v_mfma_f32_16x16x32_f16 v[38:41], v[148:151], v[168:171], v[38:41]
	v_mfma_f32_16x16x32_f16 v[34:37], v[148:151], v[172:175], v[34:37]
	s_add_u32 m0, s49, 0x6000
	v_lshl_add_u64 v[124:125], v[68:69], 0, s[0:1]
	global_load_lds_dwordx4 v[124:125], off
	v_mfma_f32_16x16x32_f16 v[30:33], v[152:155], v[160:163], v[30:33]
	v_mfma_f32_16x16x32_f16 v[26:29], v[152:155], v[164:167], v[26:29]
	v_mfma_f32_16x16x32_f16 v[22:25], v[152:155], v[168:171], v[22:25]
	s_add_u32 m0, s49, 0x8000
	v_lshl_add_u64 v[124:125], v[72:73], 0, s[0:1]
	global_load_lds_dwordx4 v[124:125], off
	v_mfma_f32_16x16x32_f16 v[18:21], v[152:155], v[172:175], v[18:21]
	v_mfma_f32_16x16x32_f16 v[14:17], v[156:159], v[160:163], v[14:17]
	v_mfma_f32_16x16x32_f16 v[10:13], v[156:159], v[164:167], v[10:13]
	s_add_u32 m0, s49, 0xa000
	v_lshl_add_u64 v[124:125], v[66:67], 0, s[0:1]
	global_load_lds_dwordx4 v[124:125], off
	v_mfma_f32_16x16x32_f16 v[6:9], v[156:159], v[168:171], v[6:9]
	v_mfma_f32_16x16x32_f16 v[2:5], v[156:159], v[172:175], v[2:5]
	s_add_u32 s0, s0, 0x80
	s_addc_u32 s1, s1, 0
	s_add_i32 s48, s48, 1
	s_add_i32 s49, s45, 1
	s_cmp_lg_u32 s45, 2
	s_cselect_b32 s45, s49, 0
	s_add_i32 s49, s46, 1
	s_cmp_lg_u32 s46, 2
	s_cselect_b32 s46, s49, 0
	s_waitcnt vmcnt(6)
	s_waitcnt lgkmcnt(0)
	s_barrier
	s_mul_i32 s49, s46, 0xc000
	s_add_u32 s50, s49, s3
	s_add_u32 s51, s49, s2
	v_add3_u32 v120, s50, v86, v85
	v_add3_u32 v121, s50, v86, v84
	v_add3_u32 v122, s51, v81, v85
	v_add3_u32 v123, s51, v81, v84
	s_mul_i32 s49, s45, 0xc000
	s_add_u32 s49, s49, s44
	ds_read_b128 v[88:91], v120
	ds_read_b128 v[92:95], v120 offset:2048
	ds_read_b128 v[96:99], v120 offset:4096
	ds_read_b128 v[100:103], v120 offset:6144
	v_mfma_f32_16x16x32_f16 v[62:65], v[176:179], v[192:195], v[62:65]
	ds_read_b128 v[104:107], v122
	v_mfma_f32_16x16x32_f16 v[58:61], v[176:179], v[196:199], v[58:61]
	ds_read_b128 v[108:111], v122 offset:2048
	v_mfma_f32_16x16x32_f16 v[54:57], v[176:179], v[200:203], v[54:57]
	ds_read_b128 v[112:115], v122 offset:4096
	v_mfma_f32_16x16x32_f16 v[50:53], v[176:179], v[204:207], v[50:53]
	ds_read_b128 v[116:119], v122 offset:6144
	v_mfma_f32_16x16x32_f16 v[46:49], v[180:183], v[192:195], v[46:49]
	ds_read_b128 v[144:147], v121
	v_mfma_f32_16x16x32_f16 v[42:45], v[180:183], v[196:199], v[42:45]
	ds_read_b128 v[148:151], v121 offset:2048
	v_mfma_f32_16x16x32_f16 v[38:41], v[180:183], v[200:203], v[38:41]
	ds_read_b128 v[152:155], v121 offset:4096
	v_mfma_f32_16x16x32_f16 v[34:37], v[180:183], v[204:207], v[34:37]
	ds_read_b128 v[156:159], v121 offset:6144
	v_mfma_f32_16x16x32_f16 v[30:33], v[184:187], v[192:195], v[30:33]
	ds_read_b128 v[160:163], v123
	v_mfma_f32_16x16x32_f16 v[26:29], v[184:187], v[196:199], v[26:29]
	ds_read_b128 v[164:167], v123 offset:2048
	v_mfma_f32_16x16x32_f16 v[22:25], v[184:187], v[200:203], v[22:25]
	ds_read_b128 v[168:171], v123 offset:4096
	v_mfma_f32_16x16x32_f16 v[18:21], v[184:187], v[204:207], v[18:21]
	ds_read_b128 v[172:175], v123 offset:6144
	v_mfma_f32_16x16x32_f16 v[14:17], v[188:191], v[192:195], v[14:17]
	v_mfma_f32_16x16x32_f16 v[10:13], v[188:191], v[196:199], v[10:13]
	v_mfma_f32_16x16x32_f16 v[6:9], v[188:191], v[200:203], v[6:9]
	s_mov_b32 m0, s49
	v_lshl_add_u64 v[124:125], v[76:77], 0, s[0:1]
	global_load_lds_dwordx4 v[124:125], off
	v_mfma_f32_16x16x32_f16 v[2:5], v[188:191], v[204:207], v[2:5]
	v_mfma_f32_16x16x32_f16 v[62:65], v[208:211], v[224:227], v[62:65]
	v_mfma_f32_16x16x32_f16 v[58:61], v[208:211], v[228:231], v[58:61]
	s_add_u32 m0, s49, 0x2000
	v_lshl_add_u64 v[124:125], v[74:75], 0, s[0:1]
	global_load_lds_dwordx4 v[124:125], off
	v_mfma_f32_16x16x32_f16 v[54:57], v[208:211], v[232:235], v[54:57]
	v_mfma_f32_16x16x32_f16 v[50:53], v[208:211], v[236:239], v[50:53]
	v_mfma_f32_16x16x32_f16 v[46:49], v[212:215], v[224:227], v[46:49]
	s_add_u32 m0, s49, 0x4000
	v_lshl_add_u64 v[124:125], v[70:71], 0, s[0:1]
	global_load_lds_dwordx4 v[124:125], off
	v_mfma_f32_16x16x32_f16 v[42:45], v[212:215], v[228:231], v[42:45]
	v_mfma_f32_16x16x32_f16 v[38:41], v[212:215], v[232:235], v[38:41]
	v_mfma_f32_16x16x32_f16 v[34:37], v[212:215], v[236:239], v[34:37]
	s_add_u32 m0, s49, 0x6000
	v_lshl_add_u64 v[124:125], v[68:69], 0, s[0:1]
	global_load_lds_dwordx4 v[124:125], off
	v_mfma_f32_16x16x32_f16 v[30:33], v[216:219], v[224:227], v[30:33]
	v_mfma_f32_16x16x32_f16 v[26:29], v[216:219], v[228:231], v[26:29]
	v_mfma_f32_16x16x32_f16 v[22:25], v[216:219], v[232:235], v[22:25]
	s_add_u32 m0, s49, 0x8000
	v_lshl_add_u64 v[124:125], v[72:73], 0, s[0:1]
	global_load_lds_dwordx4 v[124:125], off
	v_mfma_f32_16x16x32_f16 v[18:21], v[216:219], v[236:239], v[18:21]
	v_mfma_f32_16x16x32_f16 v[14:17], v[220:223], v[224:227], v[14:17]
	v_mfma_f32_16x16x32_f16 v[10:13], v[220:223], v[228:231], v[10:13]
	s_add_u32 m0, s49, 0xa000
	v_lshl_add_u64 v[124:125], v[66:67], 0, s[0:1]
	global_load_lds_dwordx4 v[124:125], off
	v_mfma_f32_16x16x32_f16 v[6:9], v[220:223], v[232:235], v[6:9]
	v_mfma_f32_16x16x32_f16 v[2:5], v[220:223], v[236:239], v[2:5]
	s_add_u32 s0, s0, 0x80
	s_addc_u32 s1, s1, 0
	s_add_i32 s48, s48, 1
	s_add_i32 s49, s45, 1
	s_cmp_lg_u32 s45, 2
	s_cselect_b32 s45, s49, 0
	s_add_i32 s49, s46, 1
	s_cmp_lg_u32 s46, 2
	s_cselect_b32 s46, s49, 0
	s_cmp_lt_u32 s48, 12
	s_cbranch_scc1 .LBB1_36
	s_waitcnt vmcnt(6)
	s_waitcnt lgkmcnt(0)
	s_barrier
	s_mul_i32 s49, s46, 0xc000
	s_add_u32 s50, s49, s3
	s_add_u32 s51, s49, s2
	v_add3_u32 v120, s50, v86, v85
	v_add3_u32 v121, s50, v86, v84
	v_add3_u32 v122, s51, v81, v85
	v_add3_u32 v123, s51, v81, v84
	s_mul_i32 s49, s45, 0xc000
	s_add_u32 s49, s49, s44
	ds_read_b128 v[176:179], v120
	ds_read_b128 v[180:183], v120 offset:2048
	ds_read_b128 v[184:187], v120 offset:4096
	ds_read_b128 v[188:191], v120 offset:6144
	v_mfma_f32_16x16x32_f16 v[62:65], v[88:91], v[104:107], v[62:65]
	ds_read_b128 v[192:195], v122
	v_mfma_f32_16x16x32_f16 v[58:61], v[88:91], v[108:111], v[58:61]
	ds_read_b128 v[196:199], v122 offset:2048
	v_mfma_f32_16x16x32_f16 v[54:57], v[88:91], v[112:115], v[54:57]
	ds_read_b128 v[200:203], v122 offset:4096
	v_mfma_f32_16x16x32_f16 v[50:53], v[88:91], v[116:119], v[50:53]
	ds_read_b128 v[204:207], v122 offset:6144
	v_mfma_f32_16x16x32_f16 v[46:49], v[92:95], v[104:107], v[46:49]
	ds_read_b128 v[208:211], v121
	v_mfma_f32_16x16x32_f16 v[42:45], v[92:95], v[108:111], v[42:45]
	ds_read_b128 v[212:215], v121 offset:2048
	v_mfma_f32_16x16x32_f16 v[38:41], v[92:95], v[112:115], v[38:41]
	ds_read_b128 v[216:219], v121 offset:4096
	v_mfma_f32_16x16x32_f16 v[34:37], v[92:95], v[116:119], v[34:37]
	ds_read_b128 v[220:223], v121 offset:6144
	v_mfma_f32_16x16x32_f16 v[30:33], v[96:99], v[104:107], v[30:33]
	ds_read_b128 v[224:227], v123
	v_mfma_f32_16x16x32_f16 v[26:29], v[96:99], v[108:111], v[26:29]
	ds_read_b128 v[228:231], v123 offset:2048
	v_mfma_f32_16x16x32_f16 v[22:25], v[96:99], v[112:115], v[22:25]
	ds_read_b128 v[232:235], v123 offset:4096
	v_mfma_f32_16x16x32_f16 v[18:21], v[96:99], v[116:119], v[18:21]
	ds_read_b128 v[236:239], v123 offset:6144
	v_mfma_f32_16x16x32_f16 v[14:17], v[100:103], v[104:107], v[14:17]
	v_mfma_f32_16x16x32_f16 v[10:13], v[100:103], v[108:111], v[10:13]
	v_mfma_f32_16x16x32_f16 v[6:9], v[100:103], v[112:115], v[6:9]
	s_mov_b32 m0, s49
	v_lshl_add_u64 v[124:125], v[76:77], 0, s[0:1]
	global_load_lds_dwordx4 v[124:125], off
	v_mfma_f32_16x16x32_f16 v[2:5], v[100:103], v[116:119], v[2:5]
	v_mfma_f32_16x16x32_f16 v[62:65], v[144:147], v[160:163], v[62:65]
	v_mfma_f32_16x16x32_f16 v[58:61], v[144:147], v[164:167], v[58:61]
	s_add_u32 m0, s49, 0x2000
	v_lshl_add_u64 v[124:125], v[74:75], 0, s[0:1]
	global_load_lds_dwordx4 v[124:125], off
	v_mfma_f32_16x16x32_f16 v[54:57], v[144:147], v[168:171], v[54:57]
	v_mfma_f32_16x16x32_f16 v[50:53], v[144:147], v[172:175], v[50:53]
	v_mfma_f32_16x16x32_f16 v[46:49], v[148:151], v[160:163], v[46:49]
	s_add_u32 m0, s49, 0x4000
	v_lshl_add_u64 v[124:125], v[70:71], 0, s[0:1]
	global_load_lds_dwordx4 v[124:125], off
	v_mfma_f32_16x16x32_f16 v[42:45], v[148:151], v[164:167], v[42:45]
	v_mfma_f32_16x16x32_f16 v[38:41], v[148:151], v[168:171], v[38:41]
	v_mfma_f32_16x16x32_f16 v[34:37], v[148:151], v[172:175], v[34:37]
	s_add_u32 m0, s49, 0x6000
	v_lshl_add_u64 v[124:125], v[68:69], 0, s[0:1]
	global_load_lds_dwordx4 v[124:125], off
	v_mfma_f32_16x16x32_f16 v[30:33], v[152:155], v[160:163], v[30:33]
	v_mfma_f32_16x16x32_f16 v[26:29], v[152:155], v[164:167], v[26:29]
	v_mfma_f32_16x16x32_f16 v[22:25], v[152:155], v[168:171], v[22:25]
	s_add_u32 m0, s49, 0x8000
	v_lshl_add_u64 v[124:125], v[72:73], 0, s[0:1]
	global_load_lds_dwordx4 v[124:125], off
	v_mfma_f32_16x16x32_f16 v[18:21], v[152:155], v[172:175], v[18:21]
	v_mfma_f32_16x16x32_f16 v[14:17], v[156:159], v[160:163], v[14:17]
	v_mfma_f32_16x16x32_f16 v[10:13], v[156:159], v[164:167], v[10:13]
	s_add_u32 m0, s49, 0xa000
	v_lshl_add_u64 v[124:125], v[66:67], 0, s[0:1]
	global_load_lds_dwordx4 v[124:125], off
	v_mfma_f32_16x16x32_f16 v[6:9], v[156:159], v[168:171], v[6:9]
	v_mfma_f32_16x16x32_f16 v[2:5], v[156:159], v[172:175], v[2:5]
	s_add_u32 s0, s0, 0x80
	s_addc_u32 s1, s1, 0
	s_add_i32 s48, s48, 1
	s_add_i32 s49, s45, 1
	s_cmp_lg_u32 s45, 2
	s_cselect_b32 s45, s49, 0
	s_add_i32 s49, s46, 1
	s_cmp_lg_u32 s46, 2
	s_cselect_b32 s46, s49, 0
	s_waitcnt vmcnt(6)
	s_waitcnt lgkmcnt(0)
	s_barrier
	s_mul_i32 s49, s46, 0xc000
	s_add_u32 s50, s49, s3
	s_add_u32 s51, s49, s2
	v_add3_u32 v120, s50, v86, v85
	v_add3_u32 v121, s50, v86, v84
	v_add3_u32 v122, s51, v81, v85
	v_add3_u32 v123, s51, v81, v84
	ds_read_b128 v[88:91], v120
	ds_read_b128 v[92:95], v120 offset:2048
	ds_read_b128 v[96:99], v120 offset:4096
	ds_read_b128 v[100:103], v120 offset:6144
	v_mfma_f32_16x16x32_f16 v[62:65], v[176:179], v[192:195], v[62:65]
	ds_read_b128 v[104:107], v122
	v_mfma_f32_16x16x32_f16 v[58:61], v[176:179], v[196:199], v[58:61]
	ds_read_b128 v[108:111], v122 offset:2048
	v_mfma_f32_16x16x32_f16 v[54:57], v[176:179], v[200:203], v[54:57]
	ds_read_b128 v[112:115], v122 offset:4096
	v_mfma_f32_16x16x32_f16 v[50:53], v[176:179], v[204:207], v[50:53]
	ds_read_b128 v[116:119], v122 offset:6144
	v_mfma_f32_16x16x32_f16 v[46:49], v[180:183], v[192:195], v[46:49]
	ds_read_b128 v[144:147], v121
	v_mfma_f32_16x16x32_f16 v[42:45], v[180:183], v[196:199], v[42:45]
	ds_read_b128 v[148:151], v121 offset:2048
	v_mfma_f32_16x16x32_f16 v[38:41], v[180:183], v[200:203], v[38:41]
	ds_read_b128 v[152:155], v121 offset:4096
	v_mfma_f32_16x16x32_f16 v[34:37], v[180:183], v[204:207], v[34:37]
	ds_read_b128 v[156:159], v121 offset:6144
	v_mfma_f32_16x16x32_f16 v[30:33], v[184:187], v[192:195], v[30:33]
	ds_read_b128 v[160:163], v123
	v_mfma_f32_16x16x32_f16 v[26:29], v[184:187], v[196:199], v[26:29]
	ds_read_b128 v[164:167], v123 offset:2048
	v_mfma_f32_16x16x32_f16 v[22:25], v[184:187], v[200:203], v[22:25]
	ds_read_b128 v[168:171], v123 offset:4096
	v_mfma_f32_16x16x32_f16 v[18:21], v[184:187], v[204:207], v[18:21]
	ds_read_b128 v[172:175], v123 offset:6144
	v_mfma_f32_16x16x32_f16 v[14:17], v[188:191], v[192:195], v[14:17]
	v_mfma_f32_16x16x32_f16 v[10:13], v[188:191], v[196:199], v[10:13]
	v_mfma_f32_16x16x32_f16 v[6:9], v[188:191], v[200:203], v[6:9]
	v_mfma_f32_16x16x32_f16 v[2:5], v[188:191], v[204:207], v[2:5]
	v_mfma_f32_16x16x32_f16 v[62:65], v[208:211], v[224:227], v[62:65]
	v_mfma_f32_16x16x32_f16 v[58:61], v[208:211], v[228:231], v[58:61]
	v_mfma_f32_16x16x32_f16 v[54:57], v[208:211], v[232:235], v[54:57]
	v_mfma_f32_16x16x32_f16 v[50:53], v[208:211], v[236:239], v[50:53]
	v_mfma_f32_16x16x32_f16 v[46:49], v[212:215], v[224:227], v[46:49]
	v_mfma_f32_16x16x32_f16 v[42:45], v[212:215], v[228:231], v[42:45]
	v_mfma_f32_16x16x32_f16 v[38:41], v[212:215], v[232:235], v[38:41]
	v_mfma_f32_16x16x32_f16 v[34:37], v[212:215], v[236:239], v[34:37]
	v_mfma_f32_16x16x32_f16 v[30:33], v[216:219], v[224:227], v[30:33]
	v_mfma_f32_16x16x32_f16 v[26:29], v[216:219], v[228:231], v[26:29]
	v_mfma_f32_16x16x32_f16 v[22:25], v[216:219], v[232:235], v[22:25]
	v_mfma_f32_16x16x32_f16 v[18:21], v[216:219], v[236:239], v[18:21]
	v_mfma_f32_16x16x32_f16 v[14:17], v[220:223], v[224:227], v[14:17]
	v_mfma_f32_16x16x32_f16 v[10:13], v[220:223], v[228:231], v[10:13]
	v_mfma_f32_16x16x32_f16 v[6:9], v[220:223], v[232:235], v[6:9]
	v_mfma_f32_16x16x32_f16 v[2:5], v[220:223], v[236:239], v[2:5]
	s_add_u32 s0, s0, 0x80
	s_addc_u32 s1, s1, 0
	s_add_i32 s48, s48, 1
	s_add_i32 s49, s45, 1
	s_cmp_lg_u32 s45, 2
	s_cselect_b32 s45, s49, 0
	s_add_i32 s49, s46, 1
	s_cmp_lg_u32 s46, 2
	s_cselect_b32 s46, s49, 0
	s_waitcnt vmcnt(0)
	s_waitcnt lgkmcnt(0)
	s_barrier
	s_mul_i32 s49, s46, 0xc000
	s_add_u32 s50, s49, s3
	s_add_u32 s51, s49, s2
	v_add3_u32 v120, s50, v86, v85
	v_add3_u32 v121, s50, v86, v84
	v_add3_u32 v122, s51, v81, v85
	v_add3_u32 v123, s51, v81, v84
	ds_read_b128 v[176:179], v120
	ds_read_b128 v[180:183], v120 offset:2048
	ds_read_b128 v[184:187], v120 offset:4096
	ds_read_b128 v[188:191], v120 offset:6144
	v_mfma_f32_16x16x32_f16 v[62:65], v[88:91], v[104:107], v[62:65]
	ds_read_b128 v[192:195], v122
	v_mfma_f32_16x16x32_f16 v[58:61], v[88:91], v[108:111], v[58:61]
	ds_read_b128 v[196:199], v122 offset:2048
	v_mfma_f32_16x16x32_f16 v[54:57], v[88:91], v[112:115], v[54:57]
	ds_read_b128 v[200:203], v122 offset:4096
	v_mfma_f32_16x16x32_f16 v[50:53], v[88:91], v[116:119], v[50:53]
	ds_read_b128 v[204:207], v122 offset:6144
	v_mfma_f32_16x16x32_f16 v[46:49], v[92:95], v[104:107], v[46:49]
	ds_read_b128 v[208:211], v121
	v_mfma_f32_16x16x32_f16 v[42:45], v[92:95], v[108:111], v[42:45]
	ds_read_b128 v[212:215], v121 offset:2048
	v_mfma_f32_16x16x32_f16 v[38:41], v[92:95], v[112:115], v[38:41]
	ds_read_b128 v[216:219], v121 offset:4096
	v_mfma_f32_16x16x32_f16 v[34:37], v[92:95], v[116:119], v[34:37]
	ds_read_b128 v[220:223], v121 offset:6144
	v_mfma_f32_16x16x32_f16 v[30:33], v[96:99], v[104:107], v[30:33]
	ds_read_b128 v[224:227], v123
	v_mfma_f32_16x16x32_f16 v[26:29], v[96:99], v[108:111], v[26:29]
	ds_read_b128 v[228:231], v123 offset:2048
	v_mfma_f32_16x16x32_f16 v[22:25], v[96:99], v[112:115], v[22:25]
	ds_read_b128 v[232:235], v123 offset:4096
	v_mfma_f32_16x16x32_f16 v[18:21], v[96:99], v[116:119], v[18:21]
	ds_read_b128 v[236:239], v123 offset:6144
	v_mfma_f32_16x16x32_f16 v[14:17], v[100:103], v[104:107], v[14:17]
	v_mfma_f32_16x16x32_f16 v[10:13], v[100:103], v[108:111], v[10:13]
	v_mfma_f32_16x16x32_f16 v[6:9], v[100:103], v[112:115], v[6:9]
	v_mfma_f32_16x16x32_f16 v[2:5], v[100:103], v[116:119], v[2:5]
	v_mfma_f32_16x16x32_f16 v[62:65], v[144:147], v[160:163], v[62:65]
	v_mfma_f32_16x16x32_f16 v[58:61], v[144:147], v[164:167], v[58:61]
	v_mfma_f32_16x16x32_f16 v[54:57], v[144:147], v[168:171], v[54:57]
	v_mfma_f32_16x16x32_f16 v[50:53], v[144:147], v[172:175], v[50:53]
	v_mfma_f32_16x16x32_f16 v[46:49], v[148:151], v[160:163], v[46:49]
	v_mfma_f32_16x16x32_f16 v[42:45], v[148:151], v[164:167], v[42:45]
	v_mfma_f32_16x16x32_f16 v[38:41], v[148:151], v[168:171], v[38:41]
	v_mfma_f32_16x16x32_f16 v[34:37], v[148:151], v[172:175], v[34:37]
	v_mfma_f32_16x16x32_f16 v[30:33], v[152:155], v[160:163], v[30:33]
	v_mfma_f32_16x16x32_f16 v[26:29], v[152:155], v[164:167], v[26:29]
	v_mfma_f32_16x16x32_f16 v[22:25], v[152:155], v[168:171], v[22:25]
	v_mfma_f32_16x16x32_f16 v[18:21], v[152:155], v[172:175], v[18:21]
	v_mfma_f32_16x16x32_f16 v[14:17], v[156:159], v[160:163], v[14:17]
	v_mfma_f32_16x16x32_f16 v[10:13], v[156:159], v[164:167], v[10:13]
	v_mfma_f32_16x16x32_f16 v[6:9], v[156:159], v[168:171], v[6:9]
	v_mfma_f32_16x16x32_f16 v[2:5], v[156:159], v[172:175], v[2:5]
	s_add_u32 s0, s0, 0x80
	s_addc_u32 s1, s1, 0
	s_add_i32 s48, s48, 1
	s_add_i32 s49, s45, 1
	s_cmp_lg_u32 s45, 2
	s_cselect_b32 s45, s49, 0
	s_add_i32 s49, s46, 1
	s_cmp_lg_u32 s46, 2
	s_cselect_b32 s46, s49, 0
	s_waitcnt lgkmcnt(0)
	v_mfma_f32_16x16x32_f16 v[62:65], v[176:179], v[192:195], v[62:65]
	v_mfma_f32_16x16x32_f16 v[58:61], v[176:179], v[196:199], v[58:61]
	v_mfma_f32_16x16x32_f16 v[54:57], v[176:179], v[200:203], v[54:57]
	v_mfma_f32_16x16x32_f16 v[50:53], v[176:179], v[204:207], v[50:53]
	v_mfma_f32_16x16x32_f16 v[46:49], v[180:183], v[192:195], v[46:49]
	v_mfma_f32_16x16x32_f16 v[42:45], v[180:183], v[196:199], v[42:45]
	v_mfma_f32_16x16x32_f16 v[38:41], v[180:183], v[200:203], v[38:41]
	v_mfma_f32_16x16x32_f16 v[34:37], v[180:183], v[204:207], v[34:37]
	v_mfma_f32_16x16x32_f16 v[30:33], v[184:187], v[192:195], v[30:33]
	v_mfma_f32_16x16x32_f16 v[26:29], v[184:187], v[196:199], v[26:29]
	v_mfma_f32_16x16x32_f16 v[22:25], v[184:187], v[200:203], v[22:25]
	v_mfma_f32_16x16x32_f16 v[18:21], v[184:187], v[204:207], v[18:21]
	v_mfma_f32_16x16x32_f16 v[14:17], v[188:191], v[192:195], v[14:17]
	v_mfma_f32_16x16x32_f16 v[10:13], v[188:191], v[196:199], v[10:13]
	v_mfma_f32_16x16x32_f16 v[6:9], v[188:191], v[200:203], v[6:9]
	v_mfma_f32_16x16x32_f16 v[2:5], v[188:191], v[204:207], v[2:5]
	v_mfma_f32_16x16x32_f16 v[62:65], v[208:211], v[224:227], v[62:65]
	v_mfma_f32_16x16x32_f16 v[58:61], v[208:211], v[228:231], v[58:61]
	v_mfma_f32_16x16x32_f16 v[54:57], v[208:211], v[232:235], v[54:57]
	v_mfma_f32_16x16x32_f16 v[50:53], v[208:211], v[236:239], v[50:53]
	v_mfma_f32_16x16x32_f16 v[46:49], v[212:215], v[224:227], v[46:49]
	v_mfma_f32_16x16x32_f16 v[42:45], v[212:215], v[228:231], v[42:45]
	v_mfma_f32_16x16x32_f16 v[38:41], v[212:215], v[232:235], v[38:41]
	v_mfma_f32_16x16x32_f16 v[34:37], v[212:215], v[236:239], v[34:37]
	v_mfma_f32_16x16x32_f16 v[30:33], v[216:219], v[224:227], v[30:33]
	v_mfma_f32_16x16x32_f16 v[26:29], v[216:219], v[228:231], v[26:29]
	v_mfma_f32_16x16x32_f16 v[22:25], v[216:219], v[232:235], v[22:25]
	v_mfma_f32_16x16x32_f16 v[18:21], v[216:219], v[236:239], v[18:21]
	v_mfma_f32_16x16x32_f16 v[14:17], v[220:223], v[224:227], v[14:17]
	v_mfma_f32_16x16x32_f16 v[10:13], v[220:223], v[228:231], v[10:13]
	v_mfma_f32_16x16x32_f16 v[6:9], v[220:223], v[232:235], v[6:9]
	v_mfma_f32_16x16x32_f16 v[2:5], v[220:223], v[236:239], v[2:5]
	s_setprio 0
	s_branch .Lqk_epi_start
